# attention: fold loop-invariant K/V load address math into the loop-carried pointers (14 VALU + 4 s_nop fewer per tile)
# baseline (speedup 1.0000x reference)
; __device__ __forceinline__ float swap_max(float v) { float r0, r1; swap32(v, r0, r1); return fmaxf(r0, r1); }
; #define AT_TRR(dst, off) asm volatile("ds_read_b64_tr_b16 %0, %1 offset:%c2" : "=&v"(dst) : "v"(vaddr), "i"(off) : "memory")
; #define AT_PIN() do { _Pragma("unroll") for (int g_ = 0; g_ < 4; ++g_) { __builtin_amdgcn_sched_group_barrier(0x008, 1, 0); __builtin_amdgcn_sched_group_barrier(0x400, 2, 0); __builtin_amdgcn_sched_group_barrier(0x002, 2, 0); } \
;                 __builtin_amdgcn_sched_barrier(0); } while (0)
; __device__ __forceinline__ void attn_unit(const Frame& F, const bf16* __restrict__ proj, bf16* mix, const float* relb, const float* subg, int h, int qb, float lam, float one_m_li) {
;     ...
;             float mx = fmaxf(fmaxf(p0[0], p0[1]), p1[0]), mb = fmaxf(fmaxf(p0[2], p0[3]), p1[1]); mx = fmaxf(fmaxf(mx, p1[2]), p1[3]);
; #pragma unroll
;             for (int r = 4; r < 16; r += 4) { mx = fmaxf(fmaxf(mx, p0[r]), p0[r + 1]); mb = fmaxf(fmaxf(mb, p0[r + 2]), p0[r + 3]); mx = fmaxf(fmaxf(mx, p1[r]), p1[r + 1]); mb = fmaxf(fmaxf(mb, p1[r + 2]), p1[r + 3]); }
;             mx = swap_max(fmaxf(mx, mb));
;             if (j == 0 || __any(mx > 8.0f)) {
;                 const float dl = (j == 0) ? mx : fmaxf(mx, 0.f); mrun += dl;
;                 const float alpha = __builtin_amdgcn_exp2f(-dl); lsum *= alpha;
; #pragma unroll
;                 for (int r = 0; r < 16; ++r) { p0[r] -= dl; p1[r] -= dl; negm[r] = -mrun; }
; #pragma unroll
;                 for (int eb = 0; eb < 4; ++eb)
; #pragma unroll
;                     for (int r = 0; r < 16; ++r) o[eb][r] *= alpha;
;             }
;             bf16x8 pb[4]; float lpart[4];
;     ...
;             AT_EXPBLK(0);
;             const unsigned vaddr = (unsigned)(uintptr_t)(lds + cur * STAGE + 16384 + (4 * hi + ((lane & 15) >> 2)) * 64 + ((lane >> 4) & 1) * 32 + (lane & 3) * 8);
;             s16x4 fl[2][4], fh[2][4];
;     ...
; #pragma unroll
;             for (int eb = 0; eb < 4; ++eb) { AT_TRR(fl[0][eb], eb * 4096); AT_TRR(fh[0][eb], eb * 4096 + 512); }
;     ...
;             AT_PVSTEP(0); AT_EXPBLK(1); AT_PIN();
;             AT_PVSTEP(1); AT_EXPBLK(2); AT_PIN();
;             AT_PVSTEP(2); AT_EXPBLK(3); AT_PIN();
;             AT_PVSTEP(3); __builtin_amdgcn_sched_barrier(0);
.LBB0_578:
	v_and_b32_e32 v213, 63, v32
	v_lshlrev_b32_e32 v34, 3, v32
	v_lshlrev_b32_e32 v32, 1, v32
	v_and_b32_e32 v219, 0xc0, v33
	v_and_b32_e32 v220, 32, v32
	s_nop 2
	v_max_f32_e32 v32, v1, v1
	v_max_f32_e32 v33, v0, v0
	v_max_f32_e32 v32, v33, v32
	v_max3_f32 v33, v2, v3, v17
	v_max3_f32 v32, v32, v16, v18
	v_max3_f32 v32, v32, v19, v4
	v_max3_f32 v33, v33, v6, v7
	v_max3_f32 v32, v32, v5, v20
	v_max3_f32 v33, v33, v22, v23
	v_max3_f32 v32, v32, v21, v8
	v_max3_f32 v33, v33, v10, v11
	v_max3_f32 v32, v32, v9, v24
	v_max3_f32 v33, v33, v26, v27
	v_max3_f32 v32, v32, v25, v12
	v_max3_f32 v33, v33, v14, v15
	v_max3_f32 v32, v32, v13, v28
	v_max3_f32 v33, v33, v30, v31
	v_max3_f32 v32, v32, v29, v33
	v_mov_b32_e32 v33, v32
	s_nop 1
	v_permlane32_swap_b32 v32, v33
	v_lshlrev_b32_e32 v218, 8, v187
	v_max_f32_e32 v33, v33, v33
	v_max_f32_e32 v32, v32, v32
	v_max_f32_e32 v82, v32, v33
	v_sub_f32_e32 v0, v0, v82
	v_exp_f32_e32 v84, v0
	v_add_u32_e32 v0, 0, v218
	v_and_b32_e32 v221, 24, v34
	v_sub_f32_e32 v1, v1, v82
	v_add3_u32 v0, v0, v219, v220
	v_sub_f32_e32 v2, v2, v82
	v_sub_f32_e32 v3, v3, v82
	v_sub_f32_e32 v85, v8, v82
	v_exp_f32_e64 v8, -v82
	v_exp_f32_e32 v86, v1
	v_add3_u32 v227, v0, v221, s17
	ds_read_b64_tr_b16 v[0:1], v227 offset:0
	v_sub_f32_e32 v4, v4, v82
	v_sub_f32_e32 v5, v5, v82
	v_exp_f32_e32 v96, v2
	v_exp_f32_e32 v98, v3
	ds_read_b64_tr_b16 v[2:3], v227 offset:512
	v_sub_f32_e32 v6, v6, v82
	v_sub_f32_e32 v7, v7, v82
	v_exp_f32_e32 v92, v4
	v_exp_f32_e32 v94, v5
	ds_read_b64_tr_b16 v[4:5], v227 offset:4096
	v_exp_f32_e32 v88, v6
	v_exp_f32_e32 v90, v7
	ds_read_b64_tr_b16 v[6:7], v227 offset:4608
	v_sub_f32_e32 v97, v9, v82
	v_mul_f32_e32 v64, 0, v8
	ds_read_b64_tr_b16 v[8:9], v227 offset:8192
	v_sub_f32_e32 v99, v10, v82
	v_sub_f32_e32 v100, v11, v82
	ds_read_b64_tr_b16 v[10:11], v227 offset:8704
	ds_read_b64_tr_b16 v[108:109], v227 offset:12288
	ds_read_b64_tr_b16 v[110:111], v227 offset:12800
	ds_read_b64_tr_b16 v[162:163], v227 offset:1024
	ds_read_b64_tr_b16 v[164:165], v227 offset:1536
	ds_read_b64_tr_b16 v[166:167], v227 offset:5120
	ds_read_b64_tr_b16 v[168:169], v227 offset:5632
	ds_read_b64_tr_b16 v[170:171], v227 offset:9216
	ds_read_b64_tr_b16 v[172:173], v227 offset:9728
	ds_read_b64_tr_b16 v[174:175], v227 offset:13312
	ds_read_b64_tr_b16 v[176:177], v227 offset:13824
	s_waitcnt lgkmcnt(8)
	s_lshr_b32 s10, s9, 6
	s_lshl_b32 s12, s8, 1
	s_add_i32 s11, s10, -2
	s_mov_b32 s13, 2
	s_add_i32 s14, s12, 2
	v_mov_b32_e32 v65, v64
	v_mov_b32_e32 v66, v64
	v_mov_b32_e32 v67, v64
	v_mov_b32_e32 v68, v64
	v_mov_b32_e32 v69, v64
	v_mov_b32_e32 v70, v64
	v_mov_b32_e32 v71, v64
	v_mov_b32_e32 v72, v64
	v_mov_b32_e32 v73, v64
	v_mov_b32_e32 v74, v64
	v_mov_b32_e32 v75, v64
	v_mov_b32_e32 v76, v64
	v_mov_b32_e32 v77, v64
	v_mov_b32_e32 v78, v64
	v_mov_b32_e32 v79, v64
	v_sub_f32_e32 v83, v16, v82
	v_sub_f32_e32 v87, v17, v82
	v_sub_f32_e32 v89, v18, v82
	v_sub_f32_e32 v91, v19, v82
	v_sub_f32_e32 v93, v20, v82
	v_sub_f32_e32 v95, v21, v82
	v_sub_f32_e32 v101, v22, v82
	v_sub_f32_e32 v196, v23, v82
	v_sub_f32_e32 v197, v24, v82
	v_sub_f32_e32 v198, v25, v82
	v_sub_f32_e32 v199, v26, v82
	v_sub_f32_e32 v200, v27, v82
	v_sub_f32_e32 v201, v28, v82
	v_sub_f32_e32 v202, v29, v82
	v_sub_f32_e32 v203, v30, v82
	v_sub_f32_e32 v226, v31, v82
	v_sub_f32_e32 v178, v12, v82
	v_sub_f32_e32 v179, v13, v82
	v_sub_f32_e32 v180, v14, v82
	v_sub_f32_e32 v181, v15, v82
	v_cvt_pk_bf16_f32 v104, v84, v86
	v_cvt_pk_bf16_f32 v105, v96, v98
	v_cvt_pk_bf16_f32 v106, v92, v94
	v_cvt_pk_bf16_f32 v107, v88, v90
	s_nop 1
	v_mfma_f32_32x32x16_bf16 v[48:63], v[0:3], v[104:107], v[64:79]
	v_exp_f32_e32 v100, v100
	v_mfma_f32_32x32x16_bf16 v[32:47], v[4:7], v[104:107], v[64:79]
	v_mfma_f32_32x32x16_bf16 v[16:31], v[8:11], v[104:107], v[64:79]
	v_mov_b64_e32 v[0:1], v[64:65]
	v_mov_b64_e32 v[12:13], v[76:77]
	v_mov_b64_e32 v[14:15], v[78:79]
	v_mov_b64_e32 v[8:9], v[72:73]
	v_mov_b64_e32 v[10:11], v[74:75]
	v_mov_b64_e32 v[2:3], v[66:67]
	v_mov_b64_e32 v[4:5], v[68:69]
	v_mov_b64_e32 v[6:7], v[70:71]
	v_exp_f32_e32 v72, v181
	v_exp_f32_e32 v76, v179
	v_exp_f32_e32 v70, v180
	v_exp_f32_e32 v78, v99
	v_exp_f32_e32 v74, v178
	v_mfma_f32_32x32x16_bf16 v[0:15], v[108:111], v[104:107], v[0:15]
	v_exp_f32_e32 v66, v85
	v_exp_f32_e32 v68, v97
	v_cvt_pk_bf16_f32 v105, v78, v100
	v_cvt_pk_bf16_f32 v106, v74, v76
	v_cvt_pk_bf16_f32 v107, v70, v72
	v_cvt_pk_bf16_f32 v104, v66, v68
	ds_read_b64_tr_b16 v[108:109], v227 offset:2048
	ds_read_b64_tr_b16 v[110:111], v227 offset:2560
	ds_read_b64_tr_b16 v[178:179], v227 offset:6144
	ds_read_b64_tr_b16 v[180:181], v227 offset:6656
	ds_read_b64_tr_b16 v[182:183], v227 offset:10240
	ds_read_b64_tr_b16 v[184:185], v227 offset:10752
	ds_read_b64_tr_b16 v[222:223], v227 offset:14336
	ds_read_b64_tr_b16 v[224:225], v227 offset:14848
	s_waitcnt lgkmcnt(8)
; #define AT_PIN() do { _Pragma("unroll") for (int g_ = 0; g_ < 4; ++g_) { __builtin_amdgcn_sched_group_barrier(0x008, 1, 0); __builtin_amdgcn_sched_group_barrier(0x400, 2, 0); __builtin_amdgcn_sched_group_barrier(0x002, 2, 0); } \
;                 __builtin_amdgcn_sched_barrier(0); } while (0)
; __device__ __forceinline__ void attn_unit(const Frame& F, const bf16* __restrict__ proj, bf16* mix, const float* relb, const float* subg, int h, int qb, float lam, float one_m_li) {
;     ...
;     const bf16* kbase = proj + C_K + h * 128; const bf16* vbase = proj + C_V + h * 128;
;     ...
;             AT_PVSTEP(0); AT_EXPBLK(1); AT_PIN();
;             AT_PVSTEP(1); AT_EXPBLK(2); AT_PIN();
;             AT_PVSTEP(2); AT_EXPBLK(3); AT_PIN();
;             AT_PVSTEP(3); __builtin_amdgcn_sched_barrier(0);
;             lsum += (lpart[0] + lpart[1]) + (lpart[2] + lpart[3]);
	s_nop 1
	v_mfma_f32_32x32x16_bf16 v[48:63], v[162:165], v[104:107], v[48:63]
	v_exp_f32_e32 v85, v83
	v_exp_f32_e32 v87, v87
	s_nop 0
	v_cvt_pk_bf16_f32 v162, v85, v87
	v_mfma_f32_32x32x16_bf16 v[32:47], v[166:169], v[104:107], v[32:47]
	v_exp_f32_e32 v97, v89
	v_exp_f32_e32 v99, v91
	s_nop 0
	v_cvt_pk_bf16_f32 v163, v97, v99
	v_mfma_f32_32x32x16_bf16 v[16:31], v[170:173], v[104:107], v[16:31]
	v_exp_f32_e32 v93, v93
	v_exp_f32_e32 v95, v95
	s_nop 0
	v_cvt_pk_bf16_f32 v164, v93, v95
	v_mfma_f32_32x32x16_bf16 v[0:15], v[174:177], v[104:107], v[0:15]
	v_exp_f32_e32 v89, v101
	v_exp_f32_e32 v91, v196
	s_nop 0
	v_cvt_pk_bf16_f32 v165, v89, v91
	ds_read_b64_tr_b16 v[104:105], v227 offset:3072
	ds_read_b64_tr_b16 v[106:107], v227 offset:3584
	ds_read_b64_tr_b16 v[166:167], v227 offset:7168
	ds_read_b64_tr_b16 v[168:169], v227 offset:7680
	ds_read_b64_tr_b16 v[170:171], v227 offset:11264
	ds_read_b64_tr_b16 v[172:173], v227 offset:11776
	ds_read_b64_tr_b16 v[174:175], v227 offset:15360
	ds_read_b64_tr_b16 v[176:177], v227 offset:15872
	s_waitcnt lgkmcnt(8)
	s_nop 1
	v_mfma_f32_32x32x16_bf16 v[48:63], v[108:111], v[162:165], v[48:63]
	v_exp_f32_e32 v67, v197
	v_exp_f32_e32 v69, v198
	s_nop 0
	v_cvt_pk_bf16_f32 v108, v67, v69
	v_mfma_f32_32x32x16_bf16 v[32:47], v[178:181], v[162:165], v[32:47]
	v_exp_f32_e32 v79, v199
	v_exp_f32_e32 v101, v200
	s_nop 0
	v_cvt_pk_bf16_f32 v109, v79, v101
	v_mfma_f32_32x32x16_bf16 v[16:31], v[182:185], v[162:165], v[16:31]
	v_exp_f32_e32 v75, v201
	v_exp_f32_e32 v77, v202
	s_nop 0
	v_cvt_pk_bf16_f32 v110, v75, v77
	v_mfma_f32_32x32x16_bf16 v[0:15], v[222:225], v[162:165], v[0:15]
	v_exp_f32_e32 v71, v203
	v_exp_f32_e32 v73, v226
	s_nop 0
	v_cvt_pk_bf16_f32 v111, v71, v73
	s_waitcnt lgkmcnt(0)
	s_nop 1
	v_mfma_f32_32x32x16_bf16 v[48:63], v[104:107], v[108:111], v[48:63]
	v_mfma_f32_32x32x16_bf16 v[32:47], v[166:169], v[108:111], v[32:47]
	v_mfma_f32_32x32x16_bf16 v[16:31], v[170:173], v[108:111], v[16:31]
	v_mfma_f32_32x32x16_bf16 v[0:15], v[174:177], v[108:111], v[0:15]
	v_add_f32_e64 v96, v96, v98
	v_add_f32_e64 v97, v97, v99
	v_add_f32_e64 v92, v92, v94
	v_add_f32_e64 v93, v93, v95
	v_add_f32_e64 v88, v88, v90
	v_add_f32_e64 v89, v89, v91
	v_pk_add_f32 v[84:85], v[84:85], v[86:87]
	v_pk_add_f32 v[78:79], v[78:79], v[100:101]
	v_pk_add_f32 v[74:75], v[74:75], v[76:77]
	v_pk_add_f32 v[70:71], v[70:71], v[72:73]
	v_pk_add_f32 v[66:67], v[66:67], v[68:69]
	v_pk_add_f32 v[88:89], v[92:93], v[88:89]
	v_pk_add_f32 v[84:85], v[84:85], v[96:97]
	v_pk_add_f32 v[70:71], v[74:75], v[70:71]
	v_pk_add_f32 v[66:67], v[66:67], v[78:79]
	v_pk_add_f32 v[84:85], v[84:85], v[88:89]
	v_pk_add_f32 v[66:67], v[66:67], v[70:71]
	v_mov_b32_e32 v83, v64
	v_pk_add_f32 v[66:67], v[84:85], v[66:67]
	s_lshl_b32 s15, s8, 9
	v_pk_add_f32 v[66:67], v[66:67], v[66:67] op_sel_hi:[0,1]
	v_mov_b32_e32 v66, v193
	v_pk_add_f32 v[162:163], v[82:83], v[66:67]
	v_mad_i64_i32 v[66:67], s[8:9], v81, s21, 0
	v_pk_add_f32 v[64:65], v[162:163], 0 neg_lo:[1,1] neg_hi:[1,1]
	v_or_b32_e32 v66, v66, v80
	v_lshlrev_b32_e32 v65, 2, v102
	v_sub_u32_e32 v65, v192, v65
	v_lshl_add_u64 v[164:165], s[42:43], 0, v[66:67]
	v_mad_i64_i32 v[66:67], s[8:9], v103, s21, 0
	v_subrev_u32_e32 v65, s15, v65
	v_or_b32_e32 v66, v66, v80
	v_add_u32_e32 v222, s57, v65
	v_lshl_add_u64 v[166:167], s[42:43], 0, v[66:67]
	s_movk_i32 s60, 0xff00
	s_mov_b32 s73, 0x8000
	v_lshl_add_u64 v[164:165], v[164:165], 0, s[50:51]
	v_lshl_add_u64 v[166:167], v[166:167], 0, s[50:51]
	v_add_co_u32_e32 v164, vcc, 0x392b1c00, v164
	s_nop 1
	v_addc_co_u32_e32 v165, vcc, 0, v165, vcc
	v_add_co_u32_e32 v166, vcc, 0x392b1c00, v166
	s_nop 1
	v_addc_co_u32_e32 v167, vcc, 0, v167, vcc
	v_mov_b32_e32 v65, v64
	v_mov_b32_e32 v66, v64
	v_mov_b32_e32 v67, v64
	v_mov_b32_e32 v68, v64
	v_mov_b32_e32 v69, v64
	v_mov_b32_e32 v70, v64
	v_mov_b32_e32 v71, v64
	v_mov_b32_e32 v72, v64
	v_mov_b32_e32 v73, v64
	v_mov_b32_e32 v74, v64
	v_mov_b32_e32 v75, v64
	v_mov_b32_e32 v76, v64
	v_mov_b32_e32 v77, v64
	v_mov_b32_e32 v78, v64
	v_mov_b32_e32 v79, v64
	s_barrier
	s_branch .LBB0_581

; #define LAS __attribute__((address_space(3)))
; #define AT_LOAD(j) do { _Pragma("unroll") for (int i = 0; i < 2; ++i) { const int id = tid + 512 * i, row = id >> 4, c16 = id & 15; \
;         rk[i] = *(const u32x4*)(kbase + (size_t)(64 * (j) + row) * PW + c16 * 8); rv[i] = *(const u32x4*)(vbase + (size_t)(64 * (j) + row) * PW + c16 * 8); } } while (0)
; #define AT_STORE(buf) do { _Pragma("unroll") for (int i = 0; i < 2; ++i) { const int id = tid + 512 * i, row = id >> 4, c16 = id & 15, mk = c16 >> 3, c = c16 & 7; \
;         *(LAS u32x4*)(lds + (buf) * STAGE + mk * 8192 + c * 1024 + ((row ^ c) * 16)) = rk[i]; \
;         *(LAS u32x4*)(lds + (buf) * STAGE + 16384 + (c16 >> 2) * 4096 + row * 64 + (c16 & 3) * 16) = rv[i]; } } while (0)
; __device__ __forceinline__ void attn_unit(const Frame& F, const bf16* __restrict__ proj, bf16* mix, const float* relb, const float* subg, int h, int qb, float lam, float one_m_li) {
;     ...
;     for (int j = 0; j < NT; ++j) {
;         const int cur = j & 1;
;         bf16x8 kf[2][2];
;         const LAS unsigned char* Kb = lds + cur * STAGE + m * 8192;
;         if (j <= cw) {
; #pragma unroll
;             for (int d0 = 0; d0 < 2; ++d0) { const int c = 2 * d0 + hi; kf[d0][0] = *(const LAS bf16x8*)(Kb + c * 1024 + ((r32 ^ c) * 16)); kf[d0][1] = *(const LAS bf16x8*)(Kb + c * 1024 + ((r32 ^ c) * 16) + 512); } }
;         __builtin_amdgcn_sched_barrier(0);
;         if (j + 1 < NT) AT_STORE(cur ^ 1);
;         if (j + 2 < NT) AT_LOAD(j + 2);
.LBB0_581:
	s_and_b32 s88, s73, 0x8000
	s_add_i32 s79, s88, 0
	s_add_i32 s86, s13, -1
	s_add_i32 s87, s79, s40
	s_cmp_gt_u32 s86, s10
	s_cbranch_scc1 .Latt_idle
	v_add3_u32 v81, s87, v209, v210
	v_add3_u32 v80, s87, v211, v212
	v_add3_u32 v172, s87, v214, v215
	v_add3_u32 v173, s87, v216, v217
	ds_read_b128 v[144:147], v81
	ds_read_b128 v[148:151], v81 offset:512
	ds_read_b128 v[152:155], v80
	ds_read_b128 v[156:159], v80 offset:512
	ds_read_b128 v[168:171], v172
	ds_read_b128 v[176:179], v172 offset:512
	ds_read_b128 v[180:183], v173
	ds_read_b128 v[196:199], v173 offset:512
	s_waitcnt lgkmcnt(7)
	v_mfma_f32_32x32x16_bf16 v[96:111], v[144:147], v[112:115], v[64:79]
	s_waitcnt lgkmcnt(6)
	v_mfma_f32_32x32x16_bf16 v[80:95], v[148:151], v[112:115], v[64:79]
	s_waitcnt lgkmcnt(5)
	v_mfma_f32_32x32x16_bf16 v[96:111], v[152:155], v[116:119], v[96:111]
	s_waitcnt lgkmcnt(4)
	v_mfma_f32_32x32x16_bf16 v[80:95], v[156:159], v[116:119], v[80:95]
	s_waitcnt lgkmcnt(3)
	v_mfma_f32_32x32x16_bf16 v[96:111], v[168:171], v[120:123], v[96:111]
	s_waitcnt lgkmcnt(2)
	v_mfma_f32_32x32x16_bf16 v[80:95], v[176:179], v[120:123], v[80:95]
	s_waitcnt lgkmcnt(1)
	v_mfma_f32_32x32x16_bf16 v[96:111], v[180:183], v[124:127], v[96:111]
	s_waitcnt lgkmcnt(0)
	v_mfma_f32_32x32x16_bf16 v[80:95], v[196:199], v[124:127], v[80:95]
	s_cmp_ge_u32 s13, s14
	s_cbranch_scc1 .Latt_nostage
	s_xor_b32 s88, s88, 0x8000
	v_add3_u32 v146, s88, v189, v190
	v_add3_u32 v144, s88, v191, v204
	v_add_u32_e32 v147, v146, v207
	v_add_u32_e32 v146, v146, v205
	v_add_u32_e32 v145, v144, v208
	v_add_u32_e32 v144, v144, v206
	s_waitcnt vmcnt(3)
	ds_write_b128 v146, v[128:131]
	s_waitcnt vmcnt(2)
	ds_write_b128 v144, v[132:135] offset:16384
	s_waitcnt vmcnt(1)
	ds_write_b128 v147, v[136:139]
	s_waitcnt vmcnt(0)
	ds_write_b128 v145, v[140:143] offset:16384
	s_cmp_ge_u32 s86, s12
	s_cbranch_scc1 .Latt_st_done
	global_load_dwordx4 v[128:131], v[164:165], off
	global_load_dwordx4 v[132:135], v[164:165], off offset:1024
	global_load_dwordx4 v[136:139], v[166:167], off
	global_load_dwordx4 v[140:143], v[166:167], off offset:1024

; #define AT_LOAD(j) do { _Pragma("unroll") for (int i = 0; i < 2; ++i) { const int id = tid + 512 * i, row = id >> 4, c16 = id & 15; \
;         rk[i] = *(const u32x4*)(kbase + (size_t)(64 * (j) + row) * PW + c16 * 8); rv[i] = *(const u32x4*)(vbase + (size_t)(64 * (j) + row) * PW + c16 * 8); } } while (0)
; #define AT_STORE(buf) do { _Pragma("unroll") for (int i = 0; i < 2; ++i) { const int id = tid + 512 * i, row = id >> 4, c16 = id & 15, mk = c16 >> 3, c = c16 & 7; \
;         *(LAS u32x4*)(lds + (buf) * STAGE + mk * 8192 + c * 1024 + ((row ^ c) * 16)) = rk[i]; \
;         *(LAS u32x4*)(lds + (buf) * STAGE + 16384 + (c16 >> 2) * 4096 + row * 64 + (c16 & 3) * 16) = rv[i]; } } while (0)
; __device__ __forceinline__ void attn_unit(const Frame& F, const bf16* __restrict__ proj, bf16* mix, const float* relb, const float* subg, int h, int qb, float lam, float one_m_li) {
;     ...
;         if (j + 1 < NT) AT_STORE(cur ^ 1);
;         if (j + 2 < NT) AT_LOAD(j + 2);
.Latt_idle:
	s_cmp_ge_u32 s13, s14
	s_cbranch_scc1 .LBB0_580
	s_xor_b32 s88, s88, 0x8000
	v_add3_u32 v82, s88, v189, v190
	v_add3_u32 v80, s88, v191, v204
	v_add_u32_e32 v83, v82, v207
	v_add_u32_e32 v82, v82, v205
	v_add_u32_e32 v81, v80, v208
	v_add_u32_e32 v80, v80, v206
	s_waitcnt vmcnt(3)
	ds_write_b128 v82, v[128:131]
	s_waitcnt vmcnt(2)
	ds_write_b128 v80, v[132:135] offset:16384
	s_waitcnt vmcnt(1)
	ds_write_b128 v83, v[136:139]
	s_waitcnt vmcnt(0)
	ds_write_b128 v81, v[140:143] offset:16384
	s_cmp_ge_u32 s86, s12
	s_cbranch_scc1 .LBB0_580
	global_load_dwordx4 v[128:131], v[164:165], off
	global_load_dwordx4 v[132:135], v[164:165], off offset:1024
	global_load_dwordx4 v[136:139], v[166:167], off
	global_load_dwordx4 v[140:143], v[166:167], off offset:1024
	s_branch .LBB0_580
